# conversion tickets: 2^8 scale via packed multiplies in place, cvt dest zero-inits dropped, transposed-path address setup skipped when unused
# speedup vs baseline: 1.0221x; 1.0044x over previous
; __device__ __forceinline__ unsigned pk4_fp8(float a, float b, float c, float d) { int w = 0; w = __builtin_amdgcn_cvt_pk_fp8_f32(a, b, w, false); w = __builtin_amdgcn_cvt_pk_fp8_f32(c, d, w, true); return (unsigned)w; }
; #define LAS __attribute__((address_space(3)))
; #define lane (lane_id())
; __device__ __forceinline__ void cv8_to_lds(const f32x4 (&v)[16], LAS unsigned char* T, int wave, int lane) {
;     unsigned d[16];
; #pragma unroll
;     for (int i = 0; i < 16; ++i) d[i] = pg8::pk4_fp8(v[i].x * 256.f, v[i].y * 256.f, v[i].z * 256.f, v[i].w * 256.f);
;     unsigned o[4][4];
; #pragma unroll
;     for (int q = 0; q < 4; ++q) { const unsigned a = d[4 * q], b = d[4 * q + 1], c = d[4 * q + 2], e = d[4 * q + 3];
;         const unsigned t0 = __builtin_amdgcn_perm(b, a, 0x05010400u), t1 = __builtin_amdgcn_perm(b, a, 0x07030602u), t2 = __builtin_amdgcn_perm(e, c, 0x05010400u), t3 = __builtin_amdgcn_perm(e, c, 0x07030602u);
;         o[0][q] = __builtin_amdgcn_perm(t2, t0, 0x05040100u); o[1][q] = __builtin_amdgcn_perm(t2, t0, 0x07060302u); o[2][q] = __builtin_amdgcn_perm(t3, t1, 0x05040100u); o[3][q] = __builtin_amdgcn_perm(t3, t1, 0x07060302u); }
; #pragma unroll
;     for (int j = 0; j < 4; ++j) { v4u w; w.x = o[j][0]; w.y = o[j][1]; w.z = o[j][2]; w.w = o[j][3];
;         *(LAS v4u*)(T + (4 * lane + j) * 128 + 16 * (wave ^ (lane & 7))) = w; }
; }
.LBB0_477:
	v_bitop3_b32 v130, v132, s95, 7 bitop3:0x6c
	s_xor_b64 s[40:41], s[76:77], -1
	v_lshlrev_b32_e32 v0, 9, v132
	v_lshlrev_b32_e32 v130, 4, v130
	v_add3_u32 v130, 0, v0, v130
	s_mov_b64 s[0:1], -1
	s_and_b64 vcc, exec, s[40:41]
	s_cbranch_vccz .LBB0_479
	s_mov_b32 s0, 0x43800000
	s_waitcnt vmcnt(31)
	v_pk_mul_f32 v[66:67], v[66:67], s[0:1] op_sel_hi:[1,0]
	v_cvt_pk_fp8_f32 v136, v66, v67
	s_waitcnt vmcnt(30)
	v_pk_mul_f32 v[70:71], v[70:71], s[0:1] op_sel_hi:[1,0]
	v_cvt_pk_fp8_f32 v137, v70, v71
	v_pk_mul_f32 v[72:73], v[72:73], s[0:1] op_sel_hi:[1,0]
	v_cvt_pk_fp8_f32 v137, v72, v73 op_sel:[0,0,1]
	s_waitcnt vmcnt(29)
	v_pk_mul_f32 v[74:75], v[74:75], s[0:1] op_sel_hi:[1,0]
	v_cvt_pk_fp8_f32 v138, v74, v75
	s_waitcnt vmcnt(28)
	v_pk_mul_f32 v[78:79], v[78:79], s[0:1] op_sel_hi:[1,0]
	v_cvt_pk_fp8_f32 v139, v78, v79
	v_pk_mul_f32 v[80:81], v[80:81], s[0:1] op_sel_hi:[1,0]
	v_cvt_pk_fp8_f32 v139, v80, v81 op_sel:[0,0,1]
	s_waitcnt vmcnt(27)
	v_pk_mul_f32 v[82:83], v[82:83], s[0:1] op_sel_hi:[1,0]
	v_cvt_pk_fp8_f32 v140, v82, v83
	s_waitcnt vmcnt(26)
	v_pk_mul_f32 v[86:87], v[86:87], s[0:1] op_sel_hi:[1,0]
	v_cvt_pk_fp8_f32 v141, v86, v87
	v_pk_mul_f32 v[88:89], v[88:89], s[0:1] op_sel_hi:[1,0]
	v_cvt_pk_fp8_f32 v141, v88, v89 op_sel:[0,0,1]
	s_waitcnt vmcnt(25)
	v_pk_mul_f32 v[90:91], v[90:91], s[0:1] op_sel_hi:[1,0]
	v_cvt_pk_fp8_f32 v143, v90, v91
	s_waitcnt vmcnt(24)
	v_pk_mul_f32 v[94:95], v[94:95], s[0:1] op_sel_hi:[1,0]
	v_cvt_pk_fp8_f32 v144, v94, v95
	v_pk_mul_f32 v[96:97], v[96:97], s[0:1] op_sel_hi:[1,0]
	v_cvt_pk_fp8_f32 v144, v96, v97 op_sel:[0,0,1]
	s_waitcnt vmcnt(23)
	v_pk_mul_f32 v[98:99], v[98:99], s[0:1] op_sel_hi:[1,0]
	v_cvt_pk_fp8_f32 v145, v98, v99
	s_waitcnt vmcnt(22)
	v_pk_mul_f32 v[102:103], v[102:103], s[0:1] op_sel_hi:[1,0]
	v_cvt_pk_fp8_f32 v148, v102, v103
	v_pk_mul_f32 v[104:105], v[104:105], s[0:1] op_sel_hi:[1,0]
	v_cvt_pk_fp8_f32 v148, v104, v105 op_sel:[0,0,1]
	s_waitcnt vmcnt(21)
	v_pk_mul_f32 v[106:107], v[106:107], s[0:1] op_sel_hi:[1,0]
	v_cvt_pk_fp8_f32 v149, v106, v107
	s_waitcnt vmcnt(20)
	v_pk_mul_f32 v[110:111], v[110:111], s[0:1] op_sel_hi:[1,0]
	v_cvt_pk_fp8_f32 v150, v110, v111
	v_pk_mul_f32 v[112:113], v[112:113], s[0:1] op_sel_hi:[1,0]
	v_cvt_pk_fp8_f32 v150, v112, v113 op_sel:[0,0,1]
	s_waitcnt vmcnt(19)
	v_pk_mul_f32 v[114:115], v[114:115], s[0:1] op_sel_hi:[1,0]
	v_cvt_pk_fp8_f32 v151, v114, v115
	s_waitcnt vmcnt(18)
	v_pk_mul_f32 v[118:119], v[118:119], s[0:1] op_sel_hi:[1,0]
	v_cvt_pk_fp8_f32 v152, v118, v119
	v_pk_mul_f32 v[68:69], v[68:69], s[0:1] op_sel_hi:[1,0]
	v_cvt_pk_fp8_f32 v136, v68, v69 op_sel:[0,0,1]
	v_pk_mul_f32 v[76:77], v[76:77], s[0:1] op_sel_hi:[1,0]
	v_pk_mul_f32 v[120:121], v[120:121], s[0:1] op_sel_hi:[1,0]
	v_cvt_pk_fp8_f32 v138, v76, v77 op_sel:[0,0,1]
	v_pk_mul_f32 v[84:85], v[84:85], s[0:1] op_sel_hi:[1,0]
	v_cvt_pk_fp8_f32 v152, v120, v121 op_sel:[0,0,1]
	s_waitcnt vmcnt(17)
	v_pk_mul_f32 v[122:123], v[122:123], s[0:1] op_sel_hi:[1,0]
	v_cvt_pk_fp8_f32 v140, v84, v85 op_sel:[0,0,1]
	v_pk_mul_f32 v[92:93], v[92:93], s[0:1] op_sel_hi:[1,0]
	v_cvt_pk_fp8_f32 v153, v122, v123
	s_waitcnt vmcnt(16)
	v_pk_mul_f32 v[126:127], v[126:127], s[0:1] op_sel_hi:[1,0]
	v_cvt_pk_fp8_f32 v143, v92, v93 op_sel:[0,0,1]
	v_pk_mul_f32 v[100:101], v[100:101], s[0:1] op_sel_hi:[1,0]
	v_cvt_pk_fp8_f32 v154, v126, v127
	v_cvt_pk_fp8_f32 v145, v100, v101 op_sel:[0,0,1]
	v_pk_mul_f32 v[108:109], v[108:109], s[0:1] op_sel_hi:[1,0]
	v_cvt_pk_fp8_f32 v149, v108, v109 op_sel:[0,0,1]
	v_pk_mul_f32 v[116:117], v[116:117], s[0:1] op_sel_hi:[1,0]
	v_cvt_pk_fp8_f32 v151, v116, v117 op_sel:[0,0,1]
	v_pk_mul_f32 v[124:125], v[124:125], s[0:1] op_sel_hi:[1,0]
	v_pk_mul_f32 v[128:129], v[128:129], s[0:1] op_sel_hi:[1,0]
	v_cvt_pk_fp8_f32 v153, v124, v125 op_sel:[0,0,1]
	v_cvt_pk_fp8_f32 v154, v128, v129 op_sel:[0,0,1]
	s_mov_b32 s0, 0x5010400
	s_mov_b32 s1, 0x7030602
	v_perm_b32 v0, v137, v136, s0
	v_perm_b32 v131, v137, v136, s1
	v_perm_b32 v135, v139, v138, s0
	v_perm_b32 v136, v139, v138, s1
	s_mov_b32 s3, 0x5040100
	s_mov_b32 s2, 0x7060302
	v_perm_b32 v134, v135, v0, s3
	v_perm_b32 v138, v135, v0, s2
	v_perm_b32 v142, v136, v131, s3
	v_perm_b32 v146, v136, v131, s2
	v_perm_b32 v0, v141, v140, s0
	v_perm_b32 v131, v141, v140, s1
	v_perm_b32 v136, v144, v143, s0
	v_perm_b32 v137, v144, v143, s1
	v_perm_b32 v135, v136, v0, s3
	v_perm_b32 v139, v136, v0, s2
	v_perm_b32 v143, v137, v131, s3
	v_perm_b32 v147, v137, v131, s2
	v_perm_b32 v0, v148, v145, s0
	v_perm_b32 v131, v148, v145, s1
	v_perm_b32 v137, v150, v149, s0
	v_perm_b32 v141, v150, v149, s1
	v_perm_b32 v136, v137, v0, s3
	v_perm_b32 v140, v137, v0, s2
	v_perm_b32 v144, v141, v131, s3
	v_perm_b32 v148, v141, v131, s2
	v_perm_b32 v0, v152, v151, s0
	v_perm_b32 v141, v154, v153, s0
	v_perm_b32 v131, v152, v151, s1
	v_perm_b32 v149, v154, v153, s1
	v_perm_b32 v137, v141, v0, s3
	v_perm_b32 v141, v141, v0, s2
	v_perm_b32 v145, v149, v131, s3
	v_perm_b32 v149, v149, v131, s2
	ds_write_b128 v130, v[134:137]
	ds_write_b128 v130, v[138:141] offset:128
	ds_write_b128 v130, v[142:145] offset:256
	ds_write_b128 v130, v[146:149] offset:384
	s_waitcnt lgkmcnt(0)
	s_waitcnt lgkmcnt(0)
	s_barrier
	s_mov_b64 s[0:1], 0

; #define GAS __attribute__((address_space(1)))
; #define LAS __attribute__((address_space(3)))
; __device__ __forceinline__ unsigned pk2(float lo, float hi) { return f2bf(lo) | (f2bf(hi) << 16); }
; __device__ __forceinline__ void cv_tile_out(const CvTile& cur, LAS float* S, int tid_) {
;     ...
; #pragma unroll
;         for (int i = 0; i < 8; ++i) { const int p = tid_ + 512 * i, kc = p & 15, n = p >> 4, nn = 256 * nb + n;
;             const int drow = (cur.mode == 0) ? nn : (256 * (nn >> 7) + (nn & 127) + (cur.mode == 2 ? 128 : 0));
;             const LAS float* sp = S + (8 * kc) * LS + (n ^ (4 * (kc >> 1))); v4u o;
;             o.x = pk2(sp[0], sp[LS]); o.y = pk2(sp[2 * LS], sp[3 * LS]); o.z = pk2(sp[4 * LS], sp[5 * LS]); o.w = pk2(sp[6 * LS], sp[7 * LS]);
;             *(GAS v4u*)((bf16*)cur.WT + (size_t)drow * cur.K + 128 * kb + 8 * kc) = o; } }
.LBB0_485:
	s_mov_b32 s22, 0x8000
	s_and_b64 vcc, exec, s[14:15]
	s_cbranch_vccz .LBB0_487
	s_nop 0
	v_and_b32_e32 v70, 15, v132
	s_movk_i32 s22, 0x2080
	s_waitcnt vmcnt(21)
	v_lshlrev_b32_e32 v107, 1, v132
	v_ashrrev_i32_e32 v88, 4, v67
	v_mad_u32_u24 v106, v70, s22, 0
	v_bitop3_b32 v67, v88, v107, 28 bitop3:0x78
	v_ashrrev_i32_e32 v85, 4, v68
	v_lshl_add_u32 v86, v67, 2, v106
	v_bitop3_b32 v67, v85, v107, 28 bitop3:0x78
	v_ashrrev_i32_e32 v82, 4, v69
	v_lshl_add_u32 v83, v67, 2, v106
	v_bitop3_b32 v67, v82, v107, 28 bitop3:0x78
	v_lshl_add_u32 v80, v67, 2, v106
	v_add_u32_e32 v67, 0x800, v66
	v_ashrrev_i32_e32 v79, 4, v67
	v_bitop3_b32 v67, v79, v107, 28 bitop3:0x78
	v_lshl_add_u32 v77, v67, 2, v106
	v_add_u32_e32 v67, 0xa00, v66
	v_ashrrev_i32_e32 v76, 4, v67
	v_ashrrev_i32_e32 v104, 4, v66
	v_bitop3_b32 v67, v76, v107, 28 bitop3:0x78
	v_lshlrev_b32_e32 v105, 3, v70
	v_bitop3_b32 v70, v107, v104, 28 bitop3:0x6c
	v_lshl_add_u32 v74, v67, 2, v106
	v_add_u32_e32 v67, 0xc00, v66
	v_add_u32_e32 v66, 0xe00, v66
	v_lshl_add_u32 v95, v70, 2, v106
	v_ashrrev_i32_e32 v73, 4, v67
	v_ashrrev_i32_e32 v70, 4, v66
	v_bitop3_b32 v67, v73, v107, 28 bitop3:0x78
	v_bitop3_b32 v66, v70, v107, 28 bitop3:0x78
	v_and_b32_e32 v103, 0x7f, v104
	v_and_b32_e32 v87, 0x7f, v88
	v_and_b32_e32 v84, 0x7f, v85
	v_and_b32_e32 v81, 0x7f, v82
	v_and_b32_e32 v78, 0x7f, v79
	v_and_b32_e32 v75, 0x7f, v76
	v_and_b32_e32 v72, 0x7f, v73
	v_lshl_add_u32 v71, v67, 2, v106
	v_and_b32_e32 v69, 0x7f, v70
	v_lshl_add_u32 v68, v66, 2, v106
	s_mov_b32 s22, 0x8000
	s_and_b64 vcc, exec, s[14:15]
	v_lshlrev_b32_e32 v66, 1, v105
	s_cbranch_vccz .LBB0_487
	v_add_u32_e32 v67, s84, v104
	v_lshlrev_b32_e32 v105, 1, v67
	v_and_b32_e32 v105, 0xffffff00, v105
	v_or3_b32 v105, v103, v105, s19
	v_cndmask_b32_e64 v67, v105, v67, s[72:73]
	ds_read_b32 v105, v95
	ds_read_b32 v106, v95 offset:1040
	s_waitcnt vmcnt(20)
	v_mul_lo_u32 v112, s69, v67
	s_lshl_b64 s[40:41], s[56:57], 1
	s_mov_b32 s22, 0
	s_waitcnt lgkmcnt(1)
	v_bfe_u32 v107, v105, 16, 1
	v_add3_u32 v105, v105, v107, s10
	s_waitcnt lgkmcnt(0)
	v_bfe_u32 v107, v106, 16, 1
	v_lshrrev_b32_e32 v105, 16, v105
	v_add3_u32 v106, v106, v107, s10
	v_and_or_b32 v106, v106, s11, v105
	ds_read_b32 v105, v95 offset:2080
	ds_read_b32 v107, v95 offset:3120
	s_waitcnt lgkmcnt(1)
	v_bfe_u32 v108, v105, 16, 1
	v_add3_u32 v105, v105, v108, s10
	s_waitcnt lgkmcnt(0)
	v_bfe_u32 v108, v107, 16, 1
	v_lshrrev_b32_e32 v105, 16, v105
	v_add3_u32 v107, v107, v108, s10
	v_and_or_b32 v107, v107, s11, v105
	ds_read_b32 v105, v95 offset:4160
	ds_read_b32 v108, v95 offset:5200
	s_waitcnt lgkmcnt(1)
	v_bfe_u32 v109, v105, 16, 1
	v_add3_u32 v105, v105, v109, s10
	s_waitcnt lgkmcnt(0)
	v_bfe_u32 v109, v108, 16, 1
	v_lshrrev_b32_e32 v105, 16, v105
	v_add3_u32 v108, v108, v109, s10
	v_and_or_b32 v108, v108, s11, v105
	ds_read_b32 v105, v95 offset:6240
	ds_read_b32 v109, v95 offset:7280
	s_waitcnt lgkmcnt(1)
	v_bfe_u32 v110, v105, 16, 1
	v_add3_u32 v105, v105, v110, s10
	s_waitcnt lgkmcnt(0)
	v_bfe_u32 v110, v109, 16, 1
	v_lshrrev_b32_e32 v105, 16, v105
	v_add3_u32 v109, v109, v110, s10
	v_and_or_b32 v109, v109, s11, v105
	v_ashrrev_i32_e32 v105, 31, v67
	v_mul_lo_u32 v105, s68, v105
	v_mad_u64_u32 v[110:111], s[0:1], s68, v67, 0
	v_add3_u32 v111, v111, v105, v112
	v_lshl_add_u64 v[110:111], v[110:111], 1, s[66:67]
	v_lshl_add_u64 v[110:111], v[110:111], 0, s[40:41]
	v_mov_b32_e32 v67, v1
	v_lshl_add_u64 v[110:111], v[110:111], 0, v[66:67]
	v_add_u32_e32 v105, s84, v88
	global_store_dwordx4 v[110:111], v[106:109], off
	s_nop 1
	v_lshlrev_b32_e32 v106, 1, v105
	v_and_b32_e32 v106, 0xffffff00, v106
	v_or3_b32 v106, v87, v106, s19
	v_cndmask_b32_e64 v105, v106, v105, s[72:73]
	ds_read_b32 v106, v86
	ds_read_b32 v107, v86 offset:1040
	v_mul_lo_u32 v113, s69, v105
	s_waitcnt lgkmcnt(1)
	v_bfe_u32 v108, v106, 16, 1
	v_add3_u32 v106, v106, v108, s10
	s_waitcnt lgkmcnt(0)
	v_bfe_u32 v108, v107, 16, 1
	v_lshrrev_b32_e32 v106, 16, v106
	v_add3_u32 v107, v107, v108, s10
	v_and_or_b32 v106, v107, s11, v106
	ds_read_b32 v107, v86 offset:2080
	ds_read_b32 v108, v86 offset:3120
	s_waitcnt lgkmcnt(1)
	v_bfe_u32 v109, v107, 16, 1
	v_add3_u32 v107, v107, v109, s10
	s_waitcnt lgkmcnt(0)
	v_bfe_u32 v109, v108, 16, 1
	v_lshrrev_b32_e32 v107, 16, v107
	v_add3_u32 v108, v108, v109, s10
	v_and_or_b32 v107, v108, s11, v107
	ds_read_b32 v108, v86 offset:4160
	ds_read_b32 v109, v86 offset:5200
	s_waitcnt lgkmcnt(1)
	v_bfe_u32 v110, v108, 16, 1
	v_add3_u32 v108, v108, v110, s10
	s_waitcnt lgkmcnt(0)
	v_bfe_u32 v110, v109, 16, 1
	v_lshrrev_b32_e32 v108, 16, v108
	v_add3_u32 v109, v109, v110, s10
	v_and_or_b32 v108, v109, s11, v108
	ds_read_b32 v109, v86 offset:6240
	ds_read_b32 v110, v86 offset:7280
	s_waitcnt lgkmcnt(1)
	v_bfe_u32 v111, v109, 16, 1
	v_add3_u32 v109, v109, v111, s10
	s_waitcnt lgkmcnt(0)
	v_bfe_u32 v111, v110, 16, 1
	v_lshrrev_b32_e32 v109, 16, v109
	v_add3_u32 v110, v110, v111, s10
	v_and_or_b32 v109, v110, s11, v109
	v_ashrrev_i32_e32 v110, 31, v105
	v_mul_lo_u32 v112, s68, v110
	v_mad_u64_u32 v[110:111], s[0:1], s68, v105, 0
	v_add3_u32 v111, v111, v112, v113
	v_lshl_add_u64 v[110:111], v[110:111], 1, s[66:67]
	v_lshl_add_u64 v[110:111], v[110:111], 0, s[40:41]
	v_lshl_add_u64 v[110:111], v[110:111], 0, v[66:67]
	v_add_u32_e32 v105, s84, v85
	global_store_dwordx4 v[110:111], v[106:109], off
	s_nop 1
	v_lshlrev_b32_e32 v106, 1, v105
	v_and_b32_e32 v106, 0xffffff00, v106
	v_or3_b32 v106, v84, v106, s19
	v_cndmask_b32_e64 v105, v106, v105, s[72:73]
	ds_read_b32 v106, v83
	ds_read_b32 v107, v83 offset:1040
	v_mul_lo_u32 v113, s69, v105
	s_waitcnt lgkmcnt(1)
; #define GAS __attribute__((address_space(1)))
; #define LAS __attribute__((address_space(3)))
; __device__ __forceinline__ unsigned pk2(float lo, float hi) { return f2bf(lo) | (f2bf(hi) << 16); }
; __device__ __forceinline__ void cv_tile_out(const CvTile& cur, LAS float* S, int tid_) {
;     ...
; #pragma unroll
;         for (int i = 0; i < 8; ++i) { const int p = tid_ + 512 * i, kc = p & 15, n = p >> 4, nn = 256 * nb + n;
;             const int drow = (cur.mode == 0) ? nn : (256 * (nn >> 7) + (nn & 127) + (cur.mode == 2 ? 128 : 0));
;             const LAS float* sp = S + (8 * kc) * LS + (n ^ (4 * (kc >> 1))); v4u o;
;             o.x = pk2(sp[0], sp[LS]); o.y = pk2(sp[2 * LS], sp[3 * LS]); o.z = pk2(sp[4 * LS], sp[5 * LS]); o.w = pk2(sp[6 * LS], sp[7 * LS]);
;             *(GAS v4u*)((bf16*)cur.WT + (size_t)drow * cur.K + 128 * kb + 8 * kc) = o; } }
	v_bfe_u32 v108, v106, 16, 1
	v_add3_u32 v106, v106, v108, s10
	s_waitcnt lgkmcnt(0)
	v_bfe_u32 v108, v107, 16, 1
	v_lshrrev_b32_e32 v106, 16, v106
	v_add3_u32 v107, v107, v108, s10
	v_and_or_b32 v106, v107, s11, v106
	ds_read_b32 v107, v83 offset:2080
	ds_read_b32 v108, v83 offset:3120
	s_waitcnt lgkmcnt(1)
	v_bfe_u32 v109, v107, 16, 1
	v_add3_u32 v107, v107, v109, s10
	s_waitcnt lgkmcnt(0)
	v_bfe_u32 v109, v108, 16, 1
	v_lshrrev_b32_e32 v107, 16, v107
	v_add3_u32 v108, v108, v109, s10
	v_and_or_b32 v107, v108, s11, v107
	ds_read_b32 v108, v83 offset:4160
	ds_read_b32 v109, v83 offset:5200
	s_waitcnt lgkmcnt(1)
	v_bfe_u32 v110, v108, 16, 1
	v_add3_u32 v108, v108, v110, s10
	s_waitcnt lgkmcnt(0)
	v_bfe_u32 v110, v109, 16, 1
	v_lshrrev_b32_e32 v108, 16, v108
	v_add3_u32 v109, v109, v110, s10
	v_and_or_b32 v108, v109, s11, v108
	ds_read_b32 v109, v83 offset:6240
	ds_read_b32 v110, v83 offset:7280
	s_waitcnt lgkmcnt(1)
	v_bfe_u32 v111, v109, 16, 1
	v_add3_u32 v109, v109, v111, s10
	s_waitcnt lgkmcnt(0)
	v_bfe_u32 v111, v110, 16, 1
	v_lshrrev_b32_e32 v109, 16, v109
	v_add3_u32 v110, v110, v111, s10
	v_and_or_b32 v109, v110, s11, v109
	v_ashrrev_i32_e32 v110, 31, v105
	v_mul_lo_u32 v112, s68, v110
	v_mad_u64_u32 v[110:111], s[0:1], s68, v105, 0
	v_add3_u32 v111, v111, v112, v113
	v_lshl_add_u64 v[110:111], v[110:111], 1, s[66:67]
	v_lshl_add_u64 v[110:111], v[110:111], 0, s[40:41]
	v_lshl_add_u64 v[110:111], v[110:111], 0, v[66:67]
	v_add_u32_e32 v105, s84, v82
	global_store_dwordx4 v[110:111], v[106:109], off
	s_nop 1
	v_lshlrev_b32_e32 v106, 1, v105
	v_and_b32_e32 v106, 0xffffff00, v106
	v_or3_b32 v106, v81, v106, s19
	v_cndmask_b32_e64 v105, v106, v105, s[72:73]
	ds_read_b32 v106, v80
	ds_read_b32 v107, v80 offset:1040
	v_mul_lo_u32 v113, s69, v105
	s_waitcnt lgkmcnt(1)
	v_bfe_u32 v108, v106, 16, 1
	v_add3_u32 v106, v106, v108, s10
	s_waitcnt lgkmcnt(0)
	v_bfe_u32 v108, v107, 16, 1
	v_lshrrev_b32_e32 v106, 16, v106
	v_add3_u32 v107, v107, v108, s10
	v_and_or_b32 v106, v107, s11, v106
	ds_read_b32 v107, v80 offset:2080
	ds_read_b32 v108, v80 offset:3120
	s_waitcnt lgkmcnt(1)
	v_bfe_u32 v109, v107, 16, 1
	v_add3_u32 v107, v107, v109, s10
	s_waitcnt lgkmcnt(0)
	v_bfe_u32 v109, v108, 16, 1
	v_lshrrev_b32_e32 v107, 16, v107
	v_add3_u32 v108, v108, v109, s10
	v_and_or_b32 v107, v108, s11, v107
	ds_read_b32 v108, v80 offset:4160
	ds_read_b32 v109, v80 offset:5200
	s_waitcnt lgkmcnt(1)
	v_bfe_u32 v110, v108, 16, 1
	v_add3_u32 v108, v108, v110, s10
	s_waitcnt lgkmcnt(0)
	v_bfe_u32 v110, v109, 16, 1
	v_lshrrev_b32_e32 v108, 16, v108
	v_add3_u32 v109, v109, v110, s10
	v_and_or_b32 v108, v109, s11, v108
	ds_read_b32 v109, v80 offset:6240
	ds_read_b32 v110, v80 offset:7280
	s_waitcnt lgkmcnt(1)
	v_bfe_u32 v111, v109, 16, 1
	v_add3_u32 v109, v109, v111, s10
	s_waitcnt lgkmcnt(0)
	v_bfe_u32 v111, v110, 16, 1
	v_lshrrev_b32_e32 v109, 16, v109
	v_add3_u32 v110, v110, v111, s10
	v_and_or_b32 v109, v110, s11, v109
	v_ashrrev_i32_e32 v110, 31, v105
	v_mul_lo_u32 v112, s68, v110
	v_mad_u64_u32 v[110:111], s[0:1], s68, v105, 0
	v_add3_u32 v111, v111, v112, v113
	v_lshl_add_u64 v[110:111], v[110:111], 1, s[66:67]
	v_lshl_add_u64 v[110:111], v[110:111], 0, s[40:41]
	v_lshl_add_u64 v[110:111], v[110:111], 0, v[66:67]
	v_add_u32_e32 v105, s84, v79
	global_store_dwordx4 v[110:111], v[106:109], off
	s_nop 1
	v_lshlrev_b32_e32 v106, 1, v105
	v_and_b32_e32 v106, 0xffffff00, v106
	v_or3_b32 v106, v78, v106, s19
	v_cndmask_b32_e64 v105, v106, v105, s[72:73]
	ds_read_b32 v106, v77
	ds_read_b32 v107, v77 offset:1040
	v_mul_lo_u32 v113, s69, v105
	s_waitcnt lgkmcnt(1)
	v_bfe_u32 v108, v106, 16, 1
	v_add3_u32 v106, v106, v108, s10
	s_waitcnt lgkmcnt(0)
	v_bfe_u32 v108, v107, 16, 1
	v_lshrrev_b32_e32 v106, 16, v106
	v_add3_u32 v107, v107, v108, s10
	v_and_or_b32 v106, v107, s11, v106
	ds_read_b32 v107, v77 offset:2080
	ds_read_b32 v108, v77 offset:3120
	s_waitcnt lgkmcnt(1)
	v_bfe_u32 v109, v107, 16, 1
	v_add3_u32 v107, v107, v109, s10
	s_waitcnt lgkmcnt(0)
	v_bfe_u32 v109, v108, 16, 1
	v_lshrrev_b32_e32 v107, 16, v107
	v_add3_u32 v108, v108, v109, s10
	v_and_or_b32 v107, v108, s11, v107
	ds_read_b32 v108, v77 offset:4160
	ds_read_b32 v109, v77 offset:5200
	s_waitcnt lgkmcnt(1)
	v_bfe_u32 v110, v108, 16, 1
	v_add3_u32 v108, v108, v110, s10
	s_waitcnt lgkmcnt(0)
	v_bfe_u32 v110, v109, 16, 1
	v_lshrrev_b32_e32 v108, 16, v108
	v_add3_u32 v109, v109, v110, s10
	v_and_or_b32 v108, v109, s11, v108
	ds_read_b32 v109, v77 offset:6240
	ds_read_b32 v110, v77 offset:7280
	s_waitcnt lgkmcnt(1)
	v_bfe_u32 v111, v109, 16, 1
	v_add3_u32 v109, v109, v111, s10
	s_waitcnt lgkmcnt(0)
	v_bfe_u32 v111, v110, 16, 1
	v_lshrrev_b32_e32 v109, 16, v109
	v_add3_u32 v110, v110, v111, s10
	v_and_or_b32 v109, v110, s11, v109
	v_ashrrev_i32_e32 v110, 31, v105
	v_mul_lo_u32 v112, s68, v110
	v_mad_u64_u32 v[110:111], s[0:1], s68, v105, 0
	v_add3_u32 v111, v111, v112, v113
	v_lshl_add_u64 v[110:111], v[110:111], 1, s[66:67]
	v_lshl_add_u64 v[110:111], v[110:111], 0, s[40:41]
	v_lshl_add_u64 v[110:111], v[110:111], 0, v[66:67]
	v_add_u32_e32 v105, s84, v76
	global_store_dwordx4 v[110:111], v[106:109], off
	s_nop 1
	v_lshlrev_b32_e32 v106, 1, v105
	v_and_b32_e32 v106, 0xffffff00, v106
	v_or3_b32 v106, v75, v106, s19
	v_cndmask_b32_e64 v105, v106, v105, s[72:73]
	ds_read_b32 v106, v74
	ds_read_b32 v107, v74 offset:1040
	v_mul_lo_u32 v113, s69, v105
	s_waitcnt lgkmcnt(1)
; #define GAS __attribute__((address_space(1)))
; #define LAS __attribute__((address_space(3)))
; __device__ __forceinline__ unsigned pk2(float lo, float hi) { return f2bf(lo) | (f2bf(hi) << 16); }
; __device__ __forceinline__ void cv_tile_out(const CvTile& cur, LAS float* S, int tid_) {
;     ...
; #pragma unroll
;         for (int i = 0; i < 8; ++i) { const int p = tid_ + 512 * i, kc = p & 15, n = p >> 4, nn = 256 * nb + n;
;             const int drow = (cur.mode == 0) ? nn : (256 * (nn >> 7) + (nn & 127) + (cur.mode == 2 ? 128 : 0));
;             const LAS float* sp = S + (8 * kc) * LS + (n ^ (4 * (kc >> 1))); v4u o;
;             o.x = pk2(sp[0], sp[LS]); o.y = pk2(sp[2 * LS], sp[3 * LS]); o.z = pk2(sp[4 * LS], sp[5 * LS]); o.w = pk2(sp[6 * LS], sp[7 * LS]);
;             *(GAS v4u*)((bf16*)cur.WT + (size_t)drow * cur.K + 128 * kb + 8 * kc) = o; } }
	v_bfe_u32 v108, v106, 16, 1
	v_add3_u32 v106, v106, v108, s10
	s_waitcnt lgkmcnt(0)
	v_bfe_u32 v108, v107, 16, 1
	v_lshrrev_b32_e32 v106, 16, v106
	v_add3_u32 v107, v107, v108, s10
	v_and_or_b32 v106, v107, s11, v106
	ds_read_b32 v107, v74 offset:2080
	ds_read_b32 v108, v74 offset:3120
	s_waitcnt lgkmcnt(1)
	v_bfe_u32 v109, v107, 16, 1
	v_add3_u32 v107, v107, v109, s10
	s_waitcnt lgkmcnt(0)
	v_bfe_u32 v109, v108, 16, 1
	v_lshrrev_b32_e32 v107, 16, v107
	v_add3_u32 v108, v108, v109, s10
	v_and_or_b32 v107, v108, s11, v107
	ds_read_b32 v108, v74 offset:4160
	ds_read_b32 v109, v74 offset:5200
	s_waitcnt lgkmcnt(1)
	v_bfe_u32 v110, v108, 16, 1
	v_add3_u32 v108, v108, v110, s10
	s_waitcnt lgkmcnt(0)
	v_bfe_u32 v110, v109, 16, 1
	v_lshrrev_b32_e32 v108, 16, v108
	v_add3_u32 v109, v109, v110, s10
	v_and_or_b32 v108, v109, s11, v108
	ds_read_b32 v109, v74 offset:6240
	ds_read_b32 v110, v74 offset:7280
	s_waitcnt lgkmcnt(1)
	v_bfe_u32 v111, v109, 16, 1
	v_add3_u32 v109, v109, v111, s10
	s_waitcnt lgkmcnt(0)
	v_bfe_u32 v111, v110, 16, 1
	v_lshrrev_b32_e32 v109, 16, v109
	v_add3_u32 v110, v110, v111, s10
	v_and_or_b32 v109, v110, s11, v109
	v_ashrrev_i32_e32 v110, 31, v105
	v_mul_lo_u32 v112, s68, v110
	v_mad_u64_u32 v[110:111], s[0:1], s68, v105, 0
	v_add3_u32 v111, v111, v112, v113
	v_lshl_add_u64 v[110:111], v[110:111], 1, s[66:67]
	v_lshl_add_u64 v[110:111], v[110:111], 0, s[40:41]
	v_lshl_add_u64 v[110:111], v[110:111], 0, v[66:67]
	v_add_u32_e32 v105, s84, v73
	global_store_dwordx4 v[110:111], v[106:109], off
	s_nop 1
	v_lshlrev_b32_e32 v106, 1, v105
	v_and_b32_e32 v106, 0xffffff00, v106
	v_or3_b32 v106, v72, v106, s19
	v_cndmask_b32_e64 v105, v106, v105, s[72:73]
	ds_read_b32 v106, v71
	ds_read_b32 v107, v71 offset:1040
	v_mul_lo_u32 v113, s69, v105
	s_waitcnt lgkmcnt(1)
	v_bfe_u32 v108, v106, 16, 1
	v_add3_u32 v106, v106, v108, s10
	s_waitcnt lgkmcnt(0)
	v_bfe_u32 v108, v107, 16, 1
	v_lshrrev_b32_e32 v106, 16, v106
	v_add3_u32 v107, v107, v108, s10
	v_and_or_b32 v106, v107, s11, v106
	ds_read_b32 v107, v71 offset:2080
	ds_read_b32 v108, v71 offset:3120
	s_waitcnt lgkmcnt(1)
	v_bfe_u32 v109, v107, 16, 1
	v_add3_u32 v107, v107, v109, s10
	s_waitcnt lgkmcnt(0)
	v_bfe_u32 v109, v108, 16, 1
	v_lshrrev_b32_e32 v107, 16, v107
	v_add3_u32 v108, v108, v109, s10
	v_and_or_b32 v107, v108, s11, v107
	ds_read_b32 v108, v71 offset:4160
	ds_read_b32 v109, v71 offset:5200
	s_waitcnt lgkmcnt(1)
	v_bfe_u32 v110, v108, 16, 1
	v_add3_u32 v108, v108, v110, s10
	s_waitcnt lgkmcnt(0)
	v_bfe_u32 v110, v109, 16, 1
	v_lshrrev_b32_e32 v108, 16, v108
	v_add3_u32 v109, v109, v110, s10
	v_and_or_b32 v108, v109, s11, v108
	ds_read_b32 v109, v71 offset:6240
	ds_read_b32 v110, v71 offset:7280
	s_waitcnt lgkmcnt(1)
	v_bfe_u32 v111, v109, 16, 1
	v_add3_u32 v109, v109, v111, s10
	s_waitcnt lgkmcnt(0)
	v_bfe_u32 v111, v110, 16, 1
	v_lshrrev_b32_e32 v109, 16, v109
	v_add3_u32 v110, v110, v111, s10
	v_and_or_b32 v109, v110, s11, v109
	v_ashrrev_i32_e32 v110, 31, v105
	v_mul_lo_u32 v112, s68, v110
	v_mad_u64_u32 v[110:111], s[0:1], s68, v105, 0
	v_add3_u32 v111, v111, v112, v113
	v_lshl_add_u64 v[110:111], v[110:111], 1, s[66:67]
	v_lshl_add_u64 v[110:111], v[110:111], 0, s[40:41]
	v_lshl_add_u64 v[110:111], v[110:111], 0, v[66:67]
	v_add_u32_e32 v105, s84, v70
	global_store_dwordx4 v[110:111], v[106:109], off
	s_nop 1
	v_lshlrev_b32_e32 v106, 1, v105
	v_and_b32_e32 v106, 0xffffff00, v106
	v_or3_b32 v106, v69, v106, s19
	v_cndmask_b32_e64 v105, v106, v105, s[72:73]
	ds_read_b32 v106, v68
	ds_read_b32 v107, v68 offset:1040
	v_mul_lo_u32 v113, s69, v105
	s_waitcnt lgkmcnt(1)
	v_bfe_u32 v108, v106, 16, 1
	v_add3_u32 v106, v106, v108, s10
	s_waitcnt lgkmcnt(0)
	v_bfe_u32 v108, v107, 16, 1
	v_lshrrev_b32_e32 v106, 16, v106
	v_add3_u32 v107, v107, v108, s10
	v_and_or_b32 v106, v107, s11, v106
	ds_read_b32 v107, v68 offset:2080
	ds_read_b32 v108, v68 offset:3120
	s_waitcnt lgkmcnt(1)
	v_bfe_u32 v109, v107, 16, 1
	v_add3_u32 v107, v107, v109, s10
	s_waitcnt lgkmcnt(0)
	v_bfe_u32 v109, v108, 16, 1
	v_lshrrev_b32_e32 v107, 16, v107
	v_add3_u32 v108, v108, v109, s10
	v_and_or_b32 v107, v108, s11, v107
	ds_read_b32 v108, v68 offset:4160
	ds_read_b32 v109, v68 offset:5200
	s_waitcnt lgkmcnt(1)
	v_bfe_u32 v110, v108, 16, 1
	v_add3_u32 v108, v108, v110, s10
	s_waitcnt lgkmcnt(0)
	v_bfe_u32 v110, v109, 16, 1
	v_lshrrev_b32_e32 v108, 16, v108
	v_add3_u32 v109, v109, v110, s10
	v_and_or_b32 v108, v109, s11, v108
	ds_read_b32 v109, v68 offset:6240
	ds_read_b32 v110, v68 offset:7280
	s_waitcnt lgkmcnt(1)
	v_bfe_u32 v111, v109, 16, 1
	v_add3_u32 v109, v109, v111, s10
	s_waitcnt lgkmcnt(0)
	v_bfe_u32 v111, v110, 16, 1
	v_lshrrev_b32_e32 v109, 16, v109
	v_add3_u32 v110, v110, v111, s10
	v_and_or_b32 v109, v110, s11, v109
	v_ashrrev_i32_e32 v110, 31, v105
	v_mul_lo_u32 v112, s68, v110
	v_mad_u64_u32 v[110:111], s[0:1], s68, v105, 0
	v_add3_u32 v111, v111, v112, v113
	v_lshl_add_u64 v[110:111], v[110:111], 1, s[66:67]
	v_lshl_add_u64 v[110:111], v[110:111], 0, s[40:41]
	v_lshl_add_u64 v[110:111], v[110:111], 0, v[66:67]
	global_store_dwordx4 v[110:111], v[106:109], off
	s_waitcnt lgkmcnt(0)
	s_mov_b64 s[0:1], -1
	s_barrier

; __device__ __forceinline__ unsigned pk4_fp8(float a, float b, float c, float d) { int w = 0; w = __builtin_amdgcn_cvt_pk_fp8_f32(a, b, w, false); w = __builtin_amdgcn_cvt_pk_fp8_f32(c, d, w, true); return (unsigned)w; }
; #define LAS __attribute__((address_space(3)))
; #define lane (lane_id())
; __device__ __forceinline__ void cv8_to_lds(const f32x4 (&v)[16], LAS unsigned char* T, int wave, int lane) {
;     unsigned d[16];
; #pragma unroll
;     for (int i = 0; i < 16; ++i) d[i] = pg8::pk4_fp8(v[i].x * 256.f, v[i].y * 256.f, v[i].z * 256.f, v[i].w * 256.f);
;     unsigned o[4][4];
; #pragma unroll
;     for (int q = 0; q < 4; ++q) { const unsigned a = d[4 * q], b = d[4 * q + 1], c = d[4 * q + 2], e = d[4 * q + 3];
;         const unsigned t0 = __builtin_amdgcn_perm(b, a, 0x05010400u), t1 = __builtin_amdgcn_perm(b, a, 0x07030602u), t2 = __builtin_amdgcn_perm(e, c, 0x05010400u), t3 = __builtin_amdgcn_perm(e, c, 0x07030602u);
;         o[0][q] = __builtin_amdgcn_perm(t2, t0, 0x05040100u); o[1][q] = __builtin_amdgcn_perm(t2, t0, 0x07060302u); o[2][q] = __builtin_amdgcn_perm(t3, t1, 0x05040100u); o[3][q] = __builtin_amdgcn_perm(t3, t1, 0x07060302u); }
; #pragma unroll
;     for (int j = 0; j < 4; ++j) { v4u w; w.x = o[j][0]; w.y = o[j][1]; w.z = o[j][2]; w.w = o[j][3];
;         *(LAS v4u*)(T + (4 * lane + j) * 128 + 16 * (wave ^ (lane & 7))) = w; }
.LBB0_491:
	s_xor_b64 s[28:29], s[74:75], -1
	v_readlane_b32 s48, v254, 38
	v_readlane_b32 s50, v254, 40
	v_readlane_b32 s52, v254, 42
	v_readlane_b32 s53, v254, 43
	s_mov_b64 s[0:1], -1
	s_and_b64 vcc, exec, s[28:29]
	v_readlane_b32 s49, v254, 39
	v_readlane_b32 s51, v254, 41
	s_cbranch_vccz .LBB0_495
	s_mov_b32 s0, 0x43800000
	s_waitcnt vmcnt(15)
	v_pk_mul_f32 v[2:3], v[2:3], s[0:1] op_sel_hi:[1,0]
	v_cvt_pk_fp8_f32 v108, v2, v3
	s_waitcnt vmcnt(14)
	v_pk_mul_f32 v[6:7], v[6:7], s[0:1] op_sel_hi:[1,0]
	v_cvt_pk_fp8_f32 v109, v6, v7
	v_pk_mul_f32 v[8:9], v[8:9], s[0:1] op_sel_hi:[1,0]
	v_cvt_pk_fp8_f32 v109, v8, v9 op_sel:[0,0,1]
	s_waitcnt vmcnt(13)
	v_pk_mul_f32 v[10:11], v[10:11], s[0:1] op_sel_hi:[1,0]
	v_cvt_pk_fp8_f32 v110, v10, v11
	s_waitcnt vmcnt(12)
	v_pk_mul_f32 v[14:15], v[14:15], s[0:1] op_sel_hi:[1,0]
	v_cvt_pk_fp8_f32 v111, v14, v15
	v_pk_mul_f32 v[16:17], v[16:17], s[0:1] op_sel_hi:[1,0]
	v_cvt_pk_fp8_f32 v111, v16, v17 op_sel:[0,0,1]
	s_waitcnt vmcnt(11)
	v_pk_mul_f32 v[18:19], v[18:19], s[0:1] op_sel_hi:[1,0]
	v_cvt_pk_fp8_f32 v112, v18, v19
	s_waitcnt vmcnt(10)
	v_pk_mul_f32 v[22:23], v[22:23], s[0:1] op_sel_hi:[1,0]
	v_cvt_pk_fp8_f32 v113, v22, v23
	v_pk_mul_f32 v[24:25], v[24:25], s[0:1] op_sel_hi:[1,0]
	v_cvt_pk_fp8_f32 v113, v24, v25 op_sel:[0,0,1]
	s_waitcnt vmcnt(9)
	v_pk_mul_f32 v[26:27], v[26:27], s[0:1] op_sel_hi:[1,0]
	v_cvt_pk_fp8_f32 v115, v26, v27
	s_waitcnt vmcnt(8)
	v_pk_mul_f32 v[30:31], v[30:31], s[0:1] op_sel_hi:[1,0]
	v_cvt_pk_fp8_f32 v116, v30, v31
	v_pk_mul_f32 v[32:33], v[32:33], s[0:1] op_sel_hi:[1,0]
	v_cvt_pk_fp8_f32 v116, v32, v33 op_sel:[0,0,1]
	s_waitcnt vmcnt(7)
	v_pk_mul_f32 v[34:35], v[34:35], s[0:1] op_sel_hi:[1,0]
	v_cvt_pk_fp8_f32 v117, v34, v35
	s_waitcnt vmcnt(6)
	v_pk_mul_f32 v[38:39], v[38:39], s[0:1] op_sel_hi:[1,0]
	v_cvt_pk_fp8_f32 v120, v38, v39
	v_pk_mul_f32 v[40:41], v[40:41], s[0:1] op_sel_hi:[1,0]
	v_cvt_pk_fp8_f32 v120, v40, v41 op_sel:[0,0,1]
	s_waitcnt vmcnt(5)
	v_pk_mul_f32 v[42:43], v[42:43], s[0:1] op_sel_hi:[1,0]
	v_cvt_pk_fp8_f32 v121, v42, v43
	s_waitcnt vmcnt(4)
	v_pk_mul_f32 v[46:47], v[46:47], s[0:1] op_sel_hi:[1,0]
	v_cvt_pk_fp8_f32 v122, v46, v47
	v_pk_mul_f32 v[48:49], v[48:49], s[0:1] op_sel_hi:[1,0]
	v_cvt_pk_fp8_f32 v122, v48, v49 op_sel:[0,0,1]
	s_waitcnt vmcnt(3)
	v_pk_mul_f32 v[50:51], v[50:51], s[0:1] op_sel_hi:[1,0]
	v_cvt_pk_fp8_f32 v123, v50, v51
	s_waitcnt vmcnt(2)
	v_pk_mul_f32 v[54:55], v[54:55], s[0:1] op_sel_hi:[1,0]
	v_cvt_pk_fp8_f32 v124, v54, v55
	v_pk_mul_f32 v[4:5], v[4:5], s[0:1] op_sel_hi:[1,0]
	v_cvt_pk_fp8_f32 v108, v4, v5 op_sel:[0,0,1]
	v_pk_mul_f32 v[12:13], v[12:13], s[0:1] op_sel_hi:[1,0]
	v_pk_mul_f32 v[56:57], v[56:57], s[0:1] op_sel_hi:[1,0]
	v_cvt_pk_fp8_f32 v110, v12, v13 op_sel:[0,0,1]
	v_pk_mul_f32 v[20:21], v[20:21], s[0:1] op_sel_hi:[1,0]
	v_cvt_pk_fp8_f32 v124, v56, v57 op_sel:[0,0,1]
	s_waitcnt vmcnt(1)
	v_pk_mul_f32 v[58:59], v[58:59], s[0:1] op_sel_hi:[1,0]
	v_cvt_pk_fp8_f32 v112, v20, v21 op_sel:[0,0,1]
	v_pk_mul_f32 v[28:29], v[28:29], s[0:1] op_sel_hi:[1,0]
	v_cvt_pk_fp8_f32 v125, v58, v59
	s_waitcnt vmcnt(0)
	v_pk_mul_f32 v[62:63], v[62:63], s[0:1] op_sel_hi:[1,0]
	v_cvt_pk_fp8_f32 v115, v28, v29 op_sel:[0,0,1]
	v_pk_mul_f32 v[36:37], v[36:37], s[0:1] op_sel_hi:[1,0]
	v_cvt_pk_fp8_f32 v126, v62, v63
	v_cvt_pk_fp8_f32 v117, v36, v37 op_sel:[0,0,1]
	v_pk_mul_f32 v[44:45], v[44:45], s[0:1] op_sel_hi:[1,0]
	v_cvt_pk_fp8_f32 v121, v44, v45 op_sel:[0,0,1]
	v_pk_mul_f32 v[52:53], v[52:53], s[0:1] op_sel_hi:[1,0]
	v_cvt_pk_fp8_f32 v123, v52, v53 op_sel:[0,0,1]
	v_pk_mul_f32 v[60:61], v[60:61], s[0:1] op_sel_hi:[1,0]
	v_pk_mul_f32 v[64:65], v[64:65], s[0:1] op_sel_hi:[1,0]
	v_cvt_pk_fp8_f32 v125, v60, v61 op_sel:[0,0,1]
	v_cvt_pk_fp8_f32 v126, v64, v65 op_sel:[0,0,1]
	s_mov_b32 s0, 0x5010400
	s_mov_b32 s1, 0x7030602
	v_perm_b32 v67, v109, v108, s0
	v_perm_b32 v105, v109, v108, s1
	v_perm_b32 v107, v111, v110, s0
	v_perm_b32 v108, v111, v110, s1
	s_mov_b32 s4, 0x5040100
	s_mov_b32 s3, 0x7060302
	v_perm_b32 v106, v107, v67, s4
	v_perm_b32 v110, v107, v67, s3
	v_perm_b32 v114, v108, v105, s4
	v_perm_b32 v118, v108, v105, s3
	v_perm_b32 v67, v113, v112, s0
	v_perm_b32 v105, v113, v112, s1
	v_perm_b32 v108, v116, v115, s0
	v_perm_b32 v109, v116, v115, s1
	v_perm_b32 v107, v108, v67, s4
	v_perm_b32 v111, v108, v67, s3
	v_perm_b32 v115, v109, v105, s4
	v_perm_b32 v119, v109, v105, s3
	v_perm_b32 v67, v120, v117, s0
	v_perm_b32 v105, v120, v117, s1
	v_perm_b32 v109, v122, v121, s0
	v_perm_b32 v113, v122, v121, s1
	v_perm_b32 v108, v109, v67, s4
	v_perm_b32 v112, v109, v67, s3
	v_perm_b32 v116, v113, v105, s4
	v_perm_b32 v120, v113, v105, s3
	v_perm_b32 v67, v124, v123, s0
	v_perm_b32 v113, v126, v125, s0
	v_perm_b32 v105, v124, v123, s1
	v_perm_b32 v121, v126, v125, s1
	v_perm_b32 v109, v113, v67, s4
	v_perm_b32 v113, v113, v67, s3
	v_add_u32_e32 v67, s22, v130
	v_perm_b32 v117, v121, v105, s4
	v_perm_b32 v121, v121, v105, s3
	ds_write_b128 v67, v[106:109]
	ds_write_b128 v67, v[110:113] offset:128
	ds_write_b128 v67, v[114:117] offset:256
	ds_write_b128 v67, v[118:121] offset:384
	s_waitcnt lgkmcnt(0)
	s_waitcnt lgkmcnt(0)
	s_barrier
	s_cbranch_execz .LBB0_496
